# scan: consumer waves 1-3 start each chunk 1-3 sleep quanta late (LDS read bursts of the four waves no longer coincide)
# baseline (speedup 1.0000x reference)
; #define LAS __attribute__((address_space(3)))
; __device__ __forceinline__ void p5_scan_block(Frame& F, int sb) {
;     ...
;     for (int c = 0; c < NCH; ++c) {
;         if (F.wave < 4) {
;             const LAS float* p = inb + (c & 1) * (SC_T * 384) + 4 * q; LAS float* yo = yb + (c & 1) * (SC_T * 16) + rloc;
;             const LAS float* pv = inb + (c & 1) * (SC_T * 384) + 192 + rg * 16 + rloc;
;             f32x4 w4 = *(const LAS f32x4*)(p), r4 = *(const LAS f32x4*)(p + 64), k4 = *(const LAS f32x4*)(p + 128), a4 = *(const LAS f32x4*)(p + 256), b4 = *(const LAS f32x4*)(p + 320); float vv = pv[0];
;             f32x4 w5 = *(const LAS f32x4*)(p + 384), r5 = *(const LAS f32x4*)(p + 384 + 64), k5 = *(const LAS f32x4*)(p + 384 + 128), a5 = *(const LAS f32x4*)(p + 384 + 256), b5 = *(const LAS f32x4*)(p + 384 + 320); float v5 = pv[384];
;             float yp[16];
; #pragma unroll
;             for (int s = 0; s < SC_T; ++s) {
;                 f32x4 nw = w5, nr = r5, nk = k5, na = a5, nb = b5; float nv = v5;
;                 if (s + 2 < SC_T) { nw = *(const LAS f32x4*)(p + (s + 2) * 384); nr = *(const LAS f32x4*)(p + (s + 2) * 384 + 64); nk = *(const LAS f32x4*)(p + (s + 2) * 384 + 128);
;                     na = *(const LAS f32x4*)(p + (s + 2) * 384 + 256); nb = *(const LAS f32x4*)(p + (s + 2) * 384 + 320); nv = pv[(s + 2) * 384]; }
.LBB0_2786:
	s_lshr_b32 s44, s70, 6
	s_cmp_lt_u32 s44, 1
	s_cbranch_scc1 .Lstag_done
	s_sleep 1
	s_cmp_lt_u32 s44, 2
	s_cbranch_scc1 .Lstag_done
	s_sleep 1
	s_cmp_lt_u32 s44, 3
	s_cbranch_scc1 .Lstag_done
	s_sleep 1
